# prologue key-table items: all 16 loads of an item issued together (was one pair per wait)
# baseline (speedup 1.0000x reference)
.LBB0_29:
	s_cmpk_gt_i32 s26, 0x5ff
	s_mov_b64 s[22:23], -1
	s_cbranch_scc0 .LBB0_56
	s_cmpk_gt_u32 s26, 0x6dff
	s_cbranch_scc0 .LBB0_53
	s_cmpk_gt_u32 s26, 0xadff
	s_cbranch_scc0 .LBB0_39
	s_cmp_gt_u32 s26, 0x1adff
	s_cbranch_scc0 .LBB0_34
	s_and_b32 s22, s26, 0x7fffffc0
	s_cmp_eq_u32 s22, 0x1ae00
	s_mov_b32 s22, 0x100000
	s_cselect_b32 s22, s22, 0x180000
	s_cselect_b32 s23, s59, s61
	s_cselect_b32 s24, s58, s60
	s_add_u32 s22, s70, s22
	s_addc_u32 s48, s71, 0
	s_lshl_b32 s25, s26, 12
	s_and_b32 s49, s25, 0x3f000
	s_lshl_b32 s25, s49, 2
	s_add_u32 s24, s24, s25
	s_addc_u32 s25, s23, 0
	v_lshlrev_b32_e32 v12, 2, v34
	s_lshl_b32 s23, s49, 1
	s_add_u32 s22, s22, s23
	v_lshlrev_b32_e32 v14, 1, v34
	s_addc_u32 s23, s48, 0
	global_load_dwordx4 v[108:111], v12, s[24:25]
	global_load_dwordx4 v[112:115], v12, s[24:25] offset:16
	global_load_dwordx4 v[116:119], v12, s[24:25] offset:2048
	global_load_dwordx4 v[120:123], v12, s[24:25] offset:2064
	s_add_u32 s24, s24, 0x1000
	s_addc_u32 s25, s25, 0
	global_load_dwordx4 v[124:127], v12, s[24:25]
	global_load_dwordx4 v[128:131], v12, s[24:25] offset:16
	global_load_dwordx4 v[132:135], v12, s[24:25] offset:2048
	global_load_dwordx4 v[136:139], v12, s[24:25] offset:2064
	s_add_u32 s24, s24, 0x1000
	s_addc_u32 s25, s25, 0
	global_load_dwordx4 v[140:143], v12, s[24:25]
	global_load_dwordx4 v[144:147], v12, s[24:25] offset:16
	global_load_dwordx4 v[148:151], v12, s[24:25] offset:2048
	global_load_dwordx4 v[152:155], v12, s[24:25] offset:2064
	s_add_u32 s24, s24, 0x1000
	s_addc_u32 s25, s25, 0
	global_load_dwordx4 v[156:159], v12, s[24:25]
	global_load_dwordx4 v[160:163], v12, s[24:25] offset:16
	global_load_dwordx4 v[164:167], v12, s[24:25] offset:2048
	global_load_dwordx4 v[168:171], v12, s[24:25] offset:2064
	s_waitcnt vmcnt(14)
	v_bfe_u32 v2, v108, 16, 1
	v_bfe_u32 v3, v109, 16, 1
	v_bfe_u32 v4, v110, 16, 1
	v_bfe_u32 v5, v111, 16, 1
	v_bfe_u32 v6, v112, 16, 1
	v_bfe_u32 v7, v113, 16, 1
	v_bfe_u32 v8, v114, 16, 1
	v_bfe_u32 v9, v115, 16, 1
	v_add3_u32 v108, v108, v2, s40
	v_add3_u32 v109, v109, v3, s40
	v_add3_u32 v110, v110, v4, s40
	v_add3_u32 v111, v111, v5, s40
	v_add3_u32 v112, v112, v6, s40
	v_add3_u32 v113, v113, v7, s40
	v_add3_u32 v114, v114, v8, s40
	v_add3_u32 v115, v115, v9, s40
	v_lshrrev_b32_e32 v108, 16, v108
	v_lshrrev_b32_e32 v110, 16, v110
	v_lshrrev_b32_e32 v112, 16, v112
	v_lshrrev_b32_e32 v114, 16, v114
	v_and_or_b32 v2, v109, s41, v108
	v_and_or_b32 v3, v111, s41, v110
	v_and_or_b32 v4, v113, s41, v112
	v_and_or_b32 v5, v115, s41, v114
	global_store_dwordx4 v14, v[2:5], s[22:23]
	s_nop 1
	s_waitcnt vmcnt(12)
	v_bfe_u32 v2, v116, 16, 1
	v_bfe_u32 v3, v117, 16, 1
	v_bfe_u32 v4, v118, 16, 1
	v_bfe_u32 v5, v119, 16, 1
	v_bfe_u32 v6, v120, 16, 1
	v_bfe_u32 v7, v121, 16, 1
	v_bfe_u32 v8, v122, 16, 1
	v_bfe_u32 v9, v123, 16, 1
	v_add3_u32 v116, v116, v2, s40
	v_add3_u32 v117, v117, v3, s40
	v_add3_u32 v118, v118, v4, s40
	v_add3_u32 v119, v119, v5, s40
	v_add3_u32 v120, v120, v6, s40
	v_add3_u32 v121, v121, v7, s40
	v_add3_u32 v122, v122, v8, s40
	v_add3_u32 v123, v123, v9, s40
	v_lshrrev_b32_e32 v116, 16, v116
	v_lshrrev_b32_e32 v118, 16, v118
	v_lshrrev_b32_e32 v120, 16, v120
	v_lshrrev_b32_e32 v122, 16, v122
	v_and_or_b32 v2, v117, s41, v116
	v_and_or_b32 v3, v119, s41, v118
	v_and_or_b32 v4, v121, s41, v120
	v_and_or_b32 v5, v123, s41, v122
	global_store_dwordx4 v14, v[2:5], s[22:23] offset:1024
	s_nop 1
	s_waitcnt vmcnt(10)
	v_bfe_u32 v2, v124, 16, 1
	v_bfe_u32 v3, v125, 16, 1
	v_bfe_u32 v4, v126, 16, 1
	v_bfe_u32 v5, v127, 16, 1
	v_bfe_u32 v6, v128, 16, 1
	v_bfe_u32 v7, v129, 16, 1
	v_bfe_u32 v8, v130, 16, 1
	v_bfe_u32 v9, v131, 16, 1
	v_add3_u32 v124, v124, v2, s40
	v_add3_u32 v125, v125, v3, s40
	v_add3_u32 v126, v126, v4, s40
	v_add3_u32 v127, v127, v5, s40
	v_add3_u32 v128, v128, v6, s40
	v_add3_u32 v129, v129, v7, s40
	v_add3_u32 v130, v130, v8, s40
	v_add3_u32 v131, v131, v9, s40
	v_lshrrev_b32_e32 v124, 16, v124
	v_lshrrev_b32_e32 v126, 16, v126
	v_lshrrev_b32_e32 v128, 16, v128
	v_lshrrev_b32_e32 v130, 16, v130
	v_and_or_b32 v2, v125, s41, v124
	v_and_or_b32 v3, v127, s41, v126
	v_and_or_b32 v4, v129, s41, v128
	v_and_or_b32 v5, v131, s41, v130
	global_store_dwordx4 v14, v[2:5], s[22:23] offset:2048
	s_nop 1
	s_waitcnt vmcnt(8)
	v_bfe_u32 v2, v132, 16, 1
	v_bfe_u32 v3, v133, 16, 1
	v_bfe_u32 v4, v134, 16, 1
	v_bfe_u32 v5, v135, 16, 1
	v_bfe_u32 v6, v136, 16, 1
	v_bfe_u32 v7, v137, 16, 1
	v_bfe_u32 v8, v138, 16, 1
	v_bfe_u32 v9, v139, 16, 1
	v_add3_u32 v132, v132, v2, s40
	v_add3_u32 v133, v133, v3, s40
	v_add3_u32 v134, v134, v4, s40
	v_add3_u32 v135, v135, v5, s40
	v_add3_u32 v136, v136, v6, s40
	v_add3_u32 v137, v137, v7, s40
	v_add3_u32 v138, v138, v8, s40
	v_add3_u32 v139, v139, v9, s40
	v_lshrrev_b32_e32 v132, 16, v132
	v_lshrrev_b32_e32 v134, 16, v134
	v_lshrrev_b32_e32 v136, 16, v136
	v_lshrrev_b32_e32 v138, 16, v138
	v_and_or_b32 v2, v133, s41, v132
	v_and_or_b32 v3, v135, s41, v134
	v_and_or_b32 v4, v137, s41, v136
	v_and_or_b32 v5, v139, s41, v138
	global_store_dwordx4 v14, v[2:5], s[22:23] offset:3072
	s_nop 1
	s_waitcnt vmcnt(6)
	v_bfe_u32 v2, v140, 16, 1
	v_bfe_u32 v3, v141, 16, 1
	v_bfe_u32 v4, v142, 16, 1
	v_bfe_u32 v5, v143, 16, 1
	v_bfe_u32 v6, v144, 16, 1
	v_bfe_u32 v7, v145, 16, 1
	v_bfe_u32 v8, v146, 16, 1
	v_bfe_u32 v9, v147, 16, 1
	v_add3_u32 v140, v140, v2, s40
	v_add3_u32 v141, v141, v3, s40
	v_add3_u32 v142, v142, v4, s40
	v_add3_u32 v143, v143, v5, s40
	v_add3_u32 v144, v144, v6, s40
	v_add3_u32 v145, v145, v7, s40
	v_add3_u32 v146, v146, v8, s40
	v_add3_u32 v147, v147, v9, s40
	v_lshrrev_b32_e32 v140, 16, v140
	v_lshrrev_b32_e32 v142, 16, v142
	v_lshrrev_b32_e32 v144, 16, v144
	v_lshrrev_b32_e32 v146, 16, v146
	v_and_or_b32 v2, v141, s41, v140
	v_and_or_b32 v3, v143, s41, v142
	v_and_or_b32 v4, v145, s41, v144
	v_and_or_b32 v5, v147, s41, v146
	s_add_u32 s22, s22, 0x1000
	s_addc_u32 s23, s23, 0
	global_store_dwordx4 v14, v[2:5], s[22:23]
	s_nop 1
	s_waitcnt vmcnt(4)
	v_bfe_u32 v2, v148, 16, 1
	v_bfe_u32 v3, v149, 16, 1
	v_bfe_u32 v4, v150, 16, 1
	v_bfe_u32 v5, v151, 16, 1
	v_bfe_u32 v6, v152, 16, 1
	v_bfe_u32 v7, v153, 16, 1
	v_bfe_u32 v8, v154, 16, 1
	v_bfe_u32 v9, v155, 16, 1
	v_add3_u32 v148, v148, v2, s40
	v_add3_u32 v149, v149, v3, s40
	v_add3_u32 v150, v150, v4, s40
	v_add3_u32 v151, v151, v5, s40
	v_add3_u32 v152, v152, v6, s40
	v_add3_u32 v153, v153, v7, s40
	v_add3_u32 v154, v154, v8, s40
	v_add3_u32 v155, v155, v9, s40
	v_lshrrev_b32_e32 v148, 16, v148
	v_lshrrev_b32_e32 v150, 16, v150
	v_lshrrev_b32_e32 v152, 16, v152
	v_lshrrev_b32_e32 v154, 16, v154
	v_and_or_b32 v2, v149, s41, v148
	v_and_or_b32 v3, v151, s41, v150
	v_and_or_b32 v4, v153, s41, v152
	v_and_or_b32 v5, v155, s41, v154
	global_store_dwordx4 v14, v[2:5], s[22:23] offset:1024
	s_nop 1
	s_waitcnt vmcnt(2)
	v_bfe_u32 v2, v156, 16, 1
	v_bfe_u32 v3, v157, 16, 1
	v_bfe_u32 v4, v158, 16, 1
	v_bfe_u32 v5, v159, 16, 1
	v_bfe_u32 v6, v160, 16, 1
	v_bfe_u32 v7, v161, 16, 1
	v_bfe_u32 v8, v162, 16, 1
	v_bfe_u32 v9, v163, 16, 1
	v_add3_u32 v156, v156, v2, s40
	v_add3_u32 v157, v157, v3, s40
	v_add3_u32 v158, v158, v4, s40
	v_add3_u32 v159, v159, v5, s40
	v_add3_u32 v160, v160, v6, s40
	v_add3_u32 v161, v161, v7, s40
	v_add3_u32 v162, v162, v8, s40
	v_add3_u32 v163, v163, v9, s40
	v_lshrrev_b32_e32 v156, 16, v156
	v_lshrrev_b32_e32 v158, 16, v158
	v_lshrrev_b32_e32 v160, 16, v160
	v_lshrrev_b32_e32 v162, 16, v162
	v_and_or_b32 v2, v157, s41, v156
	v_and_or_b32 v3, v159, s41, v158
	v_and_or_b32 v4, v161, s41, v160
	v_and_or_b32 v5, v163, s41, v162
	global_store_dwordx4 v14, v[2:5], s[22:23] offset:2048
	s_nop 1
	s_waitcnt vmcnt(0)
	v_bfe_u32 v2, v164, 16, 1
	v_bfe_u32 v3, v165, 16, 1
	v_bfe_u32 v4, v166, 16, 1
	v_bfe_u32 v5, v167, 16, 1
	v_bfe_u32 v6, v168, 16, 1
	v_bfe_u32 v7, v169, 16, 1
	v_bfe_u32 v8, v170, 16, 1
	v_bfe_u32 v9, v171, 16, 1
	v_add3_u32 v164, v164, v2, s40
	v_add3_u32 v165, v165, v3, s40
	v_add3_u32 v166, v166, v4, s40
	v_add3_u32 v167, v167, v5, s40
	v_add3_u32 v168, v168, v6, s40
	v_add3_u32 v169, v169, v7, s40
	v_add3_u32 v170, v170, v8, s40
	v_add3_u32 v171, v171, v9, s40
	v_lshrrev_b32_e32 v164, 16, v164
	v_lshrrev_b32_e32 v166, 16, v166
	v_lshrrev_b32_e32 v168, 16, v168
	v_lshrrev_b32_e32 v170, 16, v170
	v_and_or_b32 v2, v165, s41, v164
	v_and_or_b32 v3, v167, s41, v166
	v_and_or_b32 v4, v169, s41, v168
	v_and_or_b32 v5, v171, s41, v170
	global_store_dwordx4 v14, v[2:5], s[22:23] offset:3072
	s_nop 1
	s_mov_b64 s[22:23], 0
